# GEMM K-loops: removed the back-to-back s_setprio 0 / s_setprio 1 pair between the two 8-MFMA groups of each phase
# speedup vs baseline: 1.0590x; 1.0590x over previous
.LBB0_330:
	v_add_u32_e32 v2, s91, v208
	v_add_u32_e32 v14, s92, v208
	ds_read_b128 v[18:21], v2
	ds_read_b128 v[22:25], v2 offset:1024
	ds_read_b128 v[26:29], v2 offset:2048
	ds_read_b128 v[30:33], v2 offset:3072
	ds_read_b128 v[2:5], v14
	ds_read_b128 v[6:9], v14 offset:1024
	ds_read_b128 v[10:13], v14 offset:2048
	ds_read_b128 v[14:17], v14 offset:3072
	s_add_i32 s10, s10, 2
	s_add_u32 s62, s28, 0x80
	s_addc_u32 s63, s29, 0
	s_and_b64 s[2:3], s[60:61], exec
	s_cselect_b32 s61, s63, s7
	s_cselect_b32 s60, s62, s6
	s_cselect_b32 s63, s31, s65
	s_cselect_b32 s62, s30, s64
	v_lshl_add_u64 v[200:201], s[28:29], 0, v[170:171]
	s_add_i32 m0, s15, 0xc000
	ds_read_b128 v[192:195], v219
	ds_read_b128 v[196:199], v219 offset:1024
	ds_read_b128 v[224:227], v219 offset:2048
	ds_read_b128 v[228:231], v219 offset:3072
	ds_read_b128 v[232:235], v219 offset:4096
	ds_read_b128 v[236:239], v219 offset:5120
	ds_read_b128 v[240:243], v219 offset:6144
	ds_read_b128 v[244:247], v219 offset:7168
	global_load_lds_dwordx4 v[200:201], off
	v_lshl_add_u64 v[200:201], s[28:29], 0, v[172:173]
	s_add_i32 m0, s15, 0xe000
	s_nop 0
	global_load_lds_dwordx4 v[200:201], off
	s_waitcnt vmcnt(8)
	s_waitcnt lgkmcnt(0)
	s_barrier
	s_setprio 1
	s_waitcnt lgkmcnt(0)
	v_mfma_scale_f32_16x16x128_f8f6f4 v[158:161], v[18:25], v[192:199], v[158:161], v220, v221 op_sel_hi:[0,0,0]
	v_mfma_scale_f32_16x16x128_f8f6f4 v[154:157], v[26:33], v[192:199], v[154:157], v220, v221 op_sel_hi:[0,0,0]
	v_mfma_scale_f32_16x16x128_f8f6f4 v[142:145], v[18:25], v[224:231], v[142:145], v220, v221 op_sel_hi:[0,0,0]
	v_mfma_scale_f32_16x16x128_f8f6f4 v[138:141], v[26:33], v[224:231], v[138:141], v220, v221 op_sel_hi:[0,0,0]
	v_mfma_scale_f32_16x16x128_f8f6f4 v[126:129], v[18:25], v[232:239], v[126:129], v220, v221 op_sel_hi:[0,0,0]
	v_mfma_scale_f32_16x16x128_f8f6f4 v[122:125], v[26:33], v[232:239], v[122:125], v220, v221 op_sel_hi:[0,0,0]
	v_mfma_scale_f32_16x16x128_f8f6f4 v[110:113], v[18:25], v[240:247], v[110:113], v220, v221 op_sel_hi:[0,0,0]
	v_mfma_scale_f32_16x16x128_f8f6f4 v[106:109], v[26:33], v[240:247], v[106:109], v220, v221 op_sel_hi:[0,0,0]
	v_mfma_scale_f32_16x16x128_f8f6f4 v[150:153], v[2:9], v[192:199], v[150:153], v220, v221 op_sel_hi:[0,0,0]
	v_mfma_scale_f32_16x16x128_f8f6f4 v[146:149], v[10:17], v[192:199], v[146:149], v220, v221 op_sel_hi:[0,0,0]
	v_mfma_scale_f32_16x16x128_f8f6f4 v[134:137], v[2:9], v[224:231], v[134:137], v220, v221 op_sel_hi:[0,0,0]
	v_mfma_scale_f32_16x16x128_f8f6f4 v[130:133], v[10:17], v[224:231], v[130:133], v220, v221 op_sel_hi:[0,0,0]
	v_mfma_scale_f32_16x16x128_f8f6f4 v[118:121], v[2:9], v[232:239], v[118:121], v220, v221 op_sel_hi:[0,0,0]
	v_mfma_scale_f32_16x16x128_f8f6f4 v[114:117], v[10:17], v[232:239], v[114:117], v220, v221 op_sel_hi:[0,0,0]
	v_mfma_scale_f32_16x16x128_f8f6f4 v[102:105], v[2:9], v[240:247], v[102:105], v220, v221 op_sel_hi:[0,0,0]
	v_mfma_scale_f32_16x16x128_f8f6f4 v[98:101], v[10:17], v[240:247], v[98:101], v220, v221 op_sel_hi:[0,0,0]
	s_setprio 0
	s_barrier
	s_add_i32 s2, s91, s14
	s_mov_b32 m0, s2
	ds_read_b128 v[224:227], v219 offset:16384
	ds_read_b128 v[228:231], v219 offset:17408
	ds_read_b128 v[232:235], v219 offset:18432
	ds_read_b128 v[236:239], v219 offset:19456
	ds_read_b128 v[240:243], v219 offset:20480
	ds_read_b128 v[244:247], v219 offset:21504
	ds_read_b128 v[210:213], v219 offset:22528
	ds_read_b128 v[214:217], v219 offset:23552
	global_load_lds_dwordx4 v162, s[62:63]
	s_add_i32 m0, s2, 0x2000
	v_mov_b32_e32 v169, v163
	s_add_u32 s2, s62, s87
	v_lshl_add_u64 v[192:193], s[62:63], 0, v[162:163]
	v_lshl_add_u64 v[194:195], s[62:63], 0, v[168:169]
	global_load_lds_dwordx4 v168, s[62:63]
	s_addc_u32 s3, s63, 0
	s_add_i32 s62, s92, s14
	s_mov_b32 m0, s62
	v_lshl_add_u64 v[200:201], s[60:61], 0, v[164:165]
	global_load_lds_dwordx4 v162, s[2:3]
	s_add_i32 m0, s62, 0x2000
	v_lshl_add_u64 v[202:203], s[60:61], 0, v[166:167]
	global_load_lds_dwordx4 v168, s[2:3]
	s_mov_b32 m0, s15
	v_lshl_add_u64 v[196:197], s[2:3], 0, v[162:163]
	global_load_lds_dwordx4 v[200:201], off
	s_mov_b32 m0, s22
	v_lshl_add_u64 v[198:199], s[2:3], 0, v[168:169]
	global_load_lds_dwordx4 v[202:203], off
	s_waitcnt vmcnt(8)
	s_waitcnt lgkmcnt(0)
	s_barrier
	s_setprio 1
	s_waitcnt lgkmcnt(0)
	v_mfma_scale_f32_16x16x128_f8f6f4 v[94:97], v[18:25], v[224:231], v[94:97], v220, v221 op_sel_hi:[0,0,0]
	v_mfma_scale_f32_16x16x128_f8f6f4 v[90:93], v[26:33], v[224:231], v[90:93], v220, v221 op_sel_hi:[0,0,0]
	v_mfma_scale_f32_16x16x128_f8f6f4 v[78:81], v[18:25], v[232:239], v[78:81], v220, v221 op_sel_hi:[0,0,0]
	v_mfma_scale_f32_16x16x128_f8f6f4 v[74:77], v[26:33], v[232:239], v[74:77], v220, v221 op_sel_hi:[0,0,0]
	v_mfma_scale_f32_16x16x128_f8f6f4 v[62:65], v[18:25], v[240:247], v[62:65], v220, v221 op_sel_hi:[0,0,0]
	v_mfma_scale_f32_16x16x128_f8f6f4 v[58:61], v[26:33], v[240:247], v[58:61], v220, v221 op_sel_hi:[0,0,0]
	v_mfma_scale_f32_16x16x128_f8f6f4 v[46:49], v[18:25], v[210:217], v[46:49], v220, v221 op_sel_hi:[0,0,0]
	v_mfma_scale_f32_16x16x128_f8f6f4 v[42:45], v[26:33], v[210:217], v[42:45], v220, v221 op_sel_hi:[0,0,0]
	v_mfma_scale_f32_16x16x128_f8f6f4 v[86:89], v[2:9], v[224:231], v[86:89], v220, v221 op_sel_hi:[0,0,0]
	v_mfma_scale_f32_16x16x128_f8f6f4 v[82:85], v[10:17], v[224:231], v[82:85], v220, v221 op_sel_hi:[0,0,0]
	v_mfma_scale_f32_16x16x128_f8f6f4 v[70:73], v[2:9], v[232:239], v[70:73], v220, v221 op_sel_hi:[0,0,0]
	v_mfma_scale_f32_16x16x128_f8f6f4 v[66:69], v[10:17], v[232:239], v[66:69], v220, v221 op_sel_hi:[0,0,0]
	v_mfma_scale_f32_16x16x128_f8f6f4 v[54:57], v[2:9], v[240:247], v[54:57], v220, v221 op_sel_hi:[0,0,0]
	v_mfma_scale_f32_16x16x128_f8f6f4 v[50:53], v[10:17], v[240:247], v[50:53], v220, v221 op_sel_hi:[0,0,0]
	v_mfma_scale_f32_16x16x128_f8f6f4 v[38:41], v[2:9], v[210:217], v[38:41], v220, v221 op_sel_hi:[0,0,0]
	v_mfma_scale_f32_16x16x128_f8f6f4 v[34:37], v[10:17], v[210:217], v[34:37], v220, v221 op_sel_hi:[0,0,0]
	s_setprio 0
	s_barrier
	s_add_i32 s62, 0, 0x18000
	s_add_i32 s63, 0, 0x1c000
	v_add_u32_e32 v14, s62, v208
	v_add_u32_e32 v30, s63, v208
	ds_read_b128 v[2:5], v14
	ds_read_b128 v[6:9], v14 offset:1024
	ds_read_b128 v[10:13], v14 offset:2048
	ds_read_b128 v[14:17], v14 offset:3072
	ds_read_b128 v[18:21], v30
	ds_read_b128 v[22:25], v30 offset:1024
	ds_read_b128 v[26:29], v30 offset:2048
	ds_read_b128 v[30:33], v30 offset:3072
	s_add_u32 s2, s60, s84
	s_addc_u32 s3, s61, s85
	s_mov_b32 m0, s23
	v_lshl_add_u64 v[174:175], s[2:3], 0, v[164:165]
	ds_read_b128 v[210:213], v219 offset:32768
	ds_read_b128 v[214:217], v219 offset:33792
	ds_read_b128 v[224:227], v219 offset:34816
	ds_read_b128 v[228:231], v219 offset:35840
	ds_read_b128 v[232:235], v219 offset:36864
	ds_read_b128 v[236:239], v219 offset:37888
	ds_read_b128 v[240:243], v219 offset:38912
	ds_read_b128 v[244:247], v219 offset:39936
	global_load_lds_dwordx4 v[174:175], off
	v_lshl_add_u64 v[174:175], s[2:3], 0, v[166:167]
	s_mov_b32 m0, s68
	s_nop 0
	global_load_lds_dwordx4 v[174:175], off
	s_waitcnt vmcnt(8)
	s_waitcnt lgkmcnt(0)
	s_barrier
	s_setprio 1
	s_waitcnt lgkmcnt(0)
	v_mfma_scale_f32_16x16x128_f8f6f4 v[158:161], v[2:9], v[210:217], v[158:161], v220, v221 op_sel_hi:[0,0,0]
	v_mfma_scale_f32_16x16x128_f8f6f4 v[154:157], v[10:17], v[210:217], v[154:157], v220, v221 op_sel_hi:[0,0,0]
	v_mfma_scale_f32_16x16x128_f8f6f4 v[142:145], v[2:9], v[224:231], v[142:145], v220, v221 op_sel_hi:[0,0,0]
	v_mfma_scale_f32_16x16x128_f8f6f4 v[138:141], v[10:17], v[224:231], v[138:141], v220, v221 op_sel_hi:[0,0,0]
	v_mfma_scale_f32_16x16x128_f8f6f4 v[126:129], v[2:9], v[232:239], v[126:129], v220, v221 op_sel_hi:[0,0,0]
	v_mfma_scale_f32_16x16x128_f8f6f4 v[122:125], v[10:17], v[232:239], v[122:125], v220, v221 op_sel_hi:[0,0,0]
	v_mfma_scale_f32_16x16x128_f8f6f4 v[110:113], v[2:9], v[240:247], v[110:113], v220, v221 op_sel_hi:[0,0,0]
	v_mfma_scale_f32_16x16x128_f8f6f4 v[106:109], v[10:17], v[240:247], v[106:109], v220, v221 op_sel_hi:[0,0,0]
	v_mfma_scale_f32_16x16x128_f8f6f4 v[150:153], v[18:25], v[210:217], v[150:153], v220, v221 op_sel_hi:[0,0,0]
	v_mfma_scale_f32_16x16x128_f8f6f4 v[146:149], v[26:33], v[210:217], v[146:149], v220, v221 op_sel_hi:[0,0,0]
	v_mfma_scale_f32_16x16x128_f8f6f4 v[134:137], v[18:25], v[224:231], v[134:137], v220, v221 op_sel_hi:[0,0,0]
	v_mfma_scale_f32_16x16x128_f8f6f4 v[130:133], v[26:33], v[224:231], v[130:133], v220, v221 op_sel_hi:[0,0,0]
	v_mfma_scale_f32_16x16x128_f8f6f4 v[118:121], v[18:25], v[232:239], v[118:121], v220, v221 op_sel_hi:[0,0,0]
	v_mfma_scale_f32_16x16x128_f8f6f4 v[114:117], v[26:33], v[232:239], v[114:117], v220, v221 op_sel_hi:[0,0,0]
	v_mfma_scale_f32_16x16x128_f8f6f4 v[102:105], v[18:25], v[240:247], v[102:105], v220, v221 op_sel_hi:[0,0,0]
	v_mfma_scale_f32_16x16x128_f8f6f4 v[98:101], v[26:33], v[240:247], v[98:101], v220, v221 op_sel_hi:[0,0,0]
	s_setprio 0
	s_barrier
	s_add_i32 s2, s62, s14
	v_lshl_add_u64 v[174:175], v[192:193], 0, s[88:89]
	s_mov_b32 m0, s2
	ds_read_b128 v[210:213], v219 offset:49152
	ds_read_b128 v[214:217], v219 offset:50176
	ds_read_b128 v[224:227], v219 offset:51200
	ds_read_b128 v[228:231], v219 offset:52224
	ds_read_b128 v[232:235], v219 offset:53248
	ds_read_b128 v[236:239], v219 offset:54272
	ds_read_b128 v[240:243], v219 offset:55296
	ds_read_b128 v[244:247], v219 offset:56320
	global_load_lds_dwordx4 v[174:175], off
	v_lshl_add_u64 v[174:175], v[194:195], 0, s[88:89]
	s_add_i32 m0, s2, 0x2000
	s_add_i32 s2, s63, s14
	global_load_lds_dwordx4 v[174:175], off
	v_lshl_add_u64 v[174:175], v[196:197], 0, s[88:89]
	s_mov_b32 m0, s2
	s_nop 0
	global_load_lds_dwordx4 v[174:175], off
	v_lshl_add_u64 v[174:175], v[198:199], 0, s[88:89]
	s_add_i32 m0, s2, 0x2000
	s_nop 0
	global_load_lds_dwordx4 v[174:175], off
	v_lshl_add_u64 v[174:175], v[200:201], 0, s[88:89]
	s_mov_b32 m0, s69
	s_nop 0
	global_load_lds_dwordx4 v[174:175], off
	v_lshl_add_u64 v[174:175], v[202:203], 0, s[88:89]
	s_mov_b32 m0, s35
	s_nop 0
	global_load_lds_dwordx4 v[174:175], off
	s_waitcnt vmcnt(8)
	s_waitcnt lgkmcnt(0)
	s_barrier
	s_setprio 1
	s_waitcnt lgkmcnt(0)
	v_mfma_scale_f32_16x16x128_f8f6f4 v[94:97], v[2:9], v[210:217], v[94:97], v220, v221 op_sel_hi:[0,0,0]
	v_mfma_scale_f32_16x16x128_f8f6f4 v[90:93], v[10:17], v[210:217], v[90:93], v220, v221 op_sel_hi:[0,0,0]
	v_mfma_scale_f32_16x16x128_f8f6f4 v[78:81], v[2:9], v[224:231], v[78:81], v220, v221 op_sel_hi:[0,0,0]
	v_mfma_scale_f32_16x16x128_f8f6f4 v[74:77], v[10:17], v[224:231], v[74:77], v220, v221 op_sel_hi:[0,0,0]
	v_mfma_scale_f32_16x16x128_f8f6f4 v[62:65], v[2:9], v[232:239], v[62:65], v220, v221 op_sel_hi:[0,0,0]
	v_mfma_scale_f32_16x16x128_f8f6f4 v[58:61], v[10:17], v[232:239], v[58:61], v220, v221 op_sel_hi:[0,0,0]
	v_mfma_scale_f32_16x16x128_f8f6f4 v[46:49], v[2:9], v[240:247], v[46:49], v220, v221 op_sel_hi:[0,0,0]
	v_mfma_scale_f32_16x16x128_f8f6f4 v[42:45], v[10:17], v[240:247], v[42:45], v220, v221 op_sel_hi:[0,0,0]
	v_mfma_scale_f32_16x16x128_f8f6f4 v[86:89], v[18:25], v[210:217], v[86:89], v220, v221 op_sel_hi:[0,0,0]
	v_mfma_scale_f32_16x16x128_f8f6f4 v[82:85], v[26:33], v[210:217], v[82:85], v220, v221 op_sel_hi:[0,0,0]
	v_mfma_scale_f32_16x16x128_f8f6f4 v[70:73], v[18:25], v[224:231], v[70:73], v220, v221 op_sel_hi:[0,0,0]
	v_mfma_scale_f32_16x16x128_f8f6f4 v[66:69], v[26:33], v[224:231], v[66:69], v220, v221 op_sel_hi:[0,0,0]
	v_mfma_scale_f32_16x16x128_f8f6f4 v[54:57], v[18:25], v[232:239], v[54:57], v220, v221 op_sel_hi:[0,0,0]
	v_mfma_scale_f32_16x16x128_f8f6f4 v[50:53], v[26:33], v[232:239], v[50:53], v220, v221 op_sel_hi:[0,0,0]
	v_mfma_scale_f32_16x16x128_f8f6f4 v[38:41], v[18:25], v[240:247], v[38:41], v220, v221 op_sel_hi:[0,0,0]
	v_mfma_scale_f32_16x16x128_f8f6f4 v[34:37], v[26:33], v[240:247], v[34:37], v220, v221 op_sel_hi:[0,0,0]
	s_setprio 0
	s_barrier
	s_add_u32 s28, s28, 0x100
	s_addc_u32 s29, s29, 0
	s_add_u32 s30, s30, 0x100
	s_addc_u32 s31, s31, 0
	s_cmp_ge_i32 s10, s86
	s_cbranch_scc1 .LBB0_350

.LBB0_890:
	s_add_i32 s10, s0, 2
	s_add_u32 s1, s52, s64
	s_addc_u32 s11, s53, s65
	s_add_u32 s28, s1, 0x100
	s_addc_u32 s1, s11, 0
	s_add_u32 s11, s87, s64
	s_addc_u32 s29, s88, s65
	s_cmp_eq_u32 s75, s0
	s_cselect_b32 s1, s5, s1
	s_cselect_b32 s0, s4, s28
	s_cselect_b32 s29, s49, s29
	s_cselect_b32 s28, s48, s11
	s_add_i32 s11, 0, 0x10000
	v_add_u32_e32 v11, s11, v183
	ds_read_b128 v[2:5], v11
	ds_read_b128 v[6:9], v11 offset:1024
	ds_read_b128 v[172:175], v11 offset:2048
	ds_read_b128 v[176:179], v11 offset:3072
	v_add_u32_e32 v11, s80, v183
	ds_read_b128 v[188:191], v11
	ds_read_b128 v[192:195], v11 offset:1024
	ds_read_b128 v[196:199], v11 offset:2048
	ds_read_b128 v[200:203], v11 offset:3072
	v_lshl_add_u64 v[168:169], v[156:157], 0, s[64:65]
	s_add_i32 m0, s15, 0xc000
	ds_read_b128 v[160:163], v185
	ds_read_b128 v[164:167], v185 offset:1024
	ds_read_b128 v[204:207], v185 offset:2048
	ds_read_b128 v[208:211], v185 offset:3072
	ds_read_b128 v[212:215], v185 offset:4096
	ds_read_b128 v[216:219], v185 offset:5120
	ds_read_b128 v[220:223], v185 offset:6144
	ds_read_b128 v[224:227], v185 offset:7168
	global_load_lds_dwordx4 v[168:169], off
	v_lshl_add_u64 v[168:169], v[158:159], 0, s[64:65]
	s_add_i32 m0, s15, 0xe000
	s_nop 0
	global_load_lds_dwordx4 v[168:169], off
	s_waitcnt vmcnt(8)
	s_waitcnt lgkmcnt(0)
	s_barrier
	s_setprio 1
	s_waitcnt lgkmcnt(0)
	v_mfma_scale_f32_16x16x128_f8f6f4 v[136:139], v[2:9], v[160:167], v[136:139], v186, v187 op_sel_hi:[0,0,0]
	v_mfma_scale_f32_16x16x128_f8f6f4 v[132:135], v[172:179], v[160:167], v[132:135], v186, v187 op_sel_hi:[0,0,0]
	v_mfma_scale_f32_16x16x128_f8f6f4 v[120:123], v[2:9], v[204:211], v[120:123], v186, v187 op_sel_hi:[0,0,0]
	v_mfma_scale_f32_16x16x128_f8f6f4 v[116:119], v[172:179], v[204:211], v[116:119], v186, v187 op_sel_hi:[0,0,0]
	v_mfma_scale_f32_16x16x128_f8f6f4 v[104:107], v[2:9], v[212:219], v[104:107], v186, v187 op_sel_hi:[0,0,0]
	v_mfma_scale_f32_16x16x128_f8f6f4 v[100:103], v[172:179], v[212:219], v[100:103], v186, v187 op_sel_hi:[0,0,0]
	v_mfma_scale_f32_16x16x128_f8f6f4 v[88:91], v[2:9], v[220:227], v[88:91], v186, v187 op_sel_hi:[0,0,0]
	v_mfma_scale_f32_16x16x128_f8f6f4 v[84:87], v[172:179], v[220:227], v[84:87], v186, v187 op_sel_hi:[0,0,0]
	v_mfma_scale_f32_16x16x128_f8f6f4 v[128:131], v[188:195], v[160:167], v[128:131], v186, v187 op_sel_hi:[0,0,0]
	v_mfma_scale_f32_16x16x128_f8f6f4 v[124:127], v[196:203], v[160:167], v[124:127], v186, v187 op_sel_hi:[0,0,0]
	v_mfma_scale_f32_16x16x128_f8f6f4 v[112:115], v[188:195], v[204:211], v[112:115], v186, v187 op_sel_hi:[0,0,0]
	v_mfma_scale_f32_16x16x128_f8f6f4 v[108:111], v[196:203], v[204:211], v[108:111], v186, v187 op_sel_hi:[0,0,0]
	v_mfma_scale_f32_16x16x128_f8f6f4 v[96:99], v[188:195], v[212:219], v[96:99], v186, v187 op_sel_hi:[0,0,0]
	v_mfma_scale_f32_16x16x128_f8f6f4 v[92:95], v[196:203], v[212:219], v[92:95], v186, v187 op_sel_hi:[0,0,0]
	v_mfma_scale_f32_16x16x128_f8f6f4 v[80:83], v[188:195], v[220:227], v[80:83], v186, v187 op_sel_hi:[0,0,0]
	v_mfma_scale_f32_16x16x128_f8f6f4 v[76:79], v[196:203], v[220:227], v[76:79], v186, v187 op_sel_hi:[0,0,0]
	s_setprio 0
	s_barrier
	s_add_i32 s11, s11, s8
	v_lshl_add_u64 v[160:161], s[28:29], 0, v[144:145]
	s_mov_b32 m0, s11
	ds_read_b128 v[204:207], v185 offset:16384
	ds_read_b128 v[208:211], v185 offset:17408
	ds_read_b128 v[212:215], v185 offset:18432
	ds_read_b128 v[216:219], v185 offset:19456
	ds_read_b128 v[220:223], v185 offset:20480
	ds_read_b128 v[224:227], v185 offset:21504
	ds_read_b128 v[228:231], v185 offset:22528
	ds_read_b128 v[232:235], v185 offset:23552
	global_load_lds_dwordx4 v[160:161], off
	s_add_i32 m0, s11, 0x2000
	v_lshl_add_u64 v[162:163], s[28:29], 0, v[140:141]
	s_add_u32 s28, s28, s9
	s_addc_u32 s29, s29, 0
	s_add_i32 s11, s80, s8
	global_load_lds_dwordx4 v[162:163], off
	v_lshl_add_u64 v[164:165], s[28:29], 0, v[144:145]
	s_mov_b32 m0, s11
	v_lshl_add_u64 v[166:167], s[28:29], 0, v[140:141]
	global_load_lds_dwordx4 v[164:165], off
	s_add_i32 m0, s11, 0x2000
	v_lshl_add_u64 v[168:169], s[0:1], 0, v[146:147]
	global_load_lds_dwordx4 v[166:167], off
	s_mov_b32 m0, s15
	v_lshl_add_u64 v[170:171], s[0:1], 0, v[142:143]
	global_load_lds_dwordx4 v[168:169], off
	s_mov_b32 m0, s33
	s_nop 0
	global_load_lds_dwordx4 v[170:171], off
	s_waitcnt vmcnt(8)
	s_waitcnt lgkmcnt(0)
	s_barrier
	s_setprio 1
	s_waitcnt lgkmcnt(0)
	v_mfma_scale_f32_16x16x128_f8f6f4 v[72:75], v[2:9], v[204:211], v[72:75], v186, v187 op_sel_hi:[0,0,0]
	v_mfma_scale_f32_16x16x128_f8f6f4 v[68:71], v[172:179], v[204:211], v[68:71], v186, v187 op_sel_hi:[0,0,0]
	v_mfma_scale_f32_16x16x128_f8f6f4 v[56:59], v[2:9], v[212:219], v[56:59], v186, v187 op_sel_hi:[0,0,0]
	v_mfma_scale_f32_16x16x128_f8f6f4 v[52:55], v[172:179], v[212:219], v[52:55], v186, v187 op_sel_hi:[0,0,0]
	v_mfma_scale_f32_16x16x128_f8f6f4 v[40:43], v[2:9], v[220:227], v[40:43], v186, v187 op_sel_hi:[0,0,0]
	v_mfma_scale_f32_16x16x128_f8f6f4 v[36:39], v[172:179], v[220:227], v[36:39], v186, v187 op_sel_hi:[0,0,0]
	v_mfma_scale_f32_16x16x128_f8f6f4 v[24:27], v[2:9], v[228:235], v[24:27], v186, v187 op_sel_hi:[0,0,0]
	v_mfma_scale_f32_16x16x128_f8f6f4 v[20:23], v[172:179], v[228:235], v[20:23], v186, v187 op_sel_hi:[0,0,0]
	v_mfma_scale_f32_16x16x128_f8f6f4 v[64:67], v[188:195], v[204:211], v[64:67], v186, v187 op_sel_hi:[0,0,0]
	v_mfma_scale_f32_16x16x128_f8f6f4 v[60:63], v[196:203], v[204:211], v[60:63], v186, v187 op_sel_hi:[0,0,0]
	v_mfma_scale_f32_16x16x128_f8f6f4 v[48:51], v[188:195], v[212:219], v[48:51], v186, v187 op_sel_hi:[0,0,0]
	v_mfma_scale_f32_16x16x128_f8f6f4 v[44:47], v[196:203], v[212:219], v[44:47], v186, v187 op_sel_hi:[0,0,0]
	v_mfma_scale_f32_16x16x128_f8f6f4 v[32:35], v[188:195], v[220:227], v[32:35], v186, v187 op_sel_hi:[0,0,0]
	v_mfma_scale_f32_16x16x128_f8f6f4 v[28:31], v[196:203], v[220:227], v[28:31], v186, v187 op_sel_hi:[0,0,0]
	v_mfma_scale_f32_16x16x128_f8f6f4 v[16:19], v[188:195], v[228:235], v[16:19], v186, v187 op_sel_hi:[0,0,0]
	v_mfma_scale_f32_16x16x128_f8f6f4 v[12:15], v[196:203], v[228:235], v[12:15], v186, v187 op_sel_hi:[0,0,0]
	s_setprio 0
	s_barrier
	s_add_i32 s11, 0, 0x18000
	s_add_i32 s28, 0, 0x1c000
	v_add_u32_e32 v2, s11, v183
	v_add_u32_e32 v11, s28, v183
	ds_read_b128 v[172:175], v2
	ds_read_b128 v[176:179], v2 offset:1024
	ds_read_b128 v[188:191], v2 offset:2048
	ds_read_b128 v[192:195], v2 offset:3072
	ds_read_b128 v[2:5], v11
	ds_read_b128 v[6:9], v11 offset:1024
	ds_read_b128 v[196:199], v11 offset:2048
	ds_read_b128 v[200:203], v11 offset:3072
	s_add_u32 s0, s0, s18
	s_addc_u32 s1, s1, s19
	s_mov_b32 m0, s34
	v_lshl_add_u64 v[180:181], s[0:1], 0, v[146:147]
	ds_read_b128 v[204:207], v185 offset:32768
	ds_read_b128 v[208:211], v185 offset:33792
	ds_read_b128 v[212:215], v185 offset:34816
	ds_read_b128 v[216:219], v185 offset:35840
	ds_read_b128 v[220:223], v185 offset:36864
	ds_read_b128 v[224:227], v185 offset:37888
	ds_read_b128 v[228:231], v185 offset:38912
	ds_read_b128 v[232:235], v185 offset:39936
	global_load_lds_dwordx4 v[180:181], off
	v_lshl_add_u64 v[180:181], s[0:1], 0, v[142:143]
	s_mov_b32 m0, s35
	s_nop 0
	global_load_lds_dwordx4 v[180:181], off
	s_waitcnt vmcnt(8)
	s_waitcnt lgkmcnt(0)
	s_barrier
	s_setprio 1
	s_waitcnt lgkmcnt(0)
	v_mfma_scale_f32_16x16x128_f8f6f4 v[136:139], v[172:179], v[204:211], v[136:139], v186, v187 op_sel_hi:[0,0,0]
	v_mfma_scale_f32_16x16x128_f8f6f4 v[132:135], v[188:195], v[204:211], v[132:135], v186, v187 op_sel_hi:[0,0,0]
	v_mfma_scale_f32_16x16x128_f8f6f4 v[120:123], v[172:179], v[212:219], v[120:123], v186, v187 op_sel_hi:[0,0,0]
	v_mfma_scale_f32_16x16x128_f8f6f4 v[116:119], v[188:195], v[212:219], v[116:119], v186, v187 op_sel_hi:[0,0,0]
	v_mfma_scale_f32_16x16x128_f8f6f4 v[104:107], v[172:179], v[220:227], v[104:107], v186, v187 op_sel_hi:[0,0,0]
	v_mfma_scale_f32_16x16x128_f8f6f4 v[100:103], v[188:195], v[220:227], v[100:103], v186, v187 op_sel_hi:[0,0,0]
	v_mfma_scale_f32_16x16x128_f8f6f4 v[88:91], v[172:179], v[228:235], v[88:91], v186, v187 op_sel_hi:[0,0,0]
	v_mfma_scale_f32_16x16x128_f8f6f4 v[84:87], v[188:195], v[228:235], v[84:87], v186, v187 op_sel_hi:[0,0,0]
	v_mfma_scale_f32_16x16x128_f8f6f4 v[128:131], v[2:9], v[204:211], v[128:131], v186, v187 op_sel_hi:[0,0,0]
	v_mfma_scale_f32_16x16x128_f8f6f4 v[124:127], v[196:203], v[204:211], v[124:127], v186, v187 op_sel_hi:[0,0,0]
	v_mfma_scale_f32_16x16x128_f8f6f4 v[112:115], v[2:9], v[212:219], v[112:115], v186, v187 op_sel_hi:[0,0,0]
	v_mfma_scale_f32_16x16x128_f8f6f4 v[108:111], v[196:203], v[212:219], v[108:111], v186, v187 op_sel_hi:[0,0,0]
	v_mfma_scale_f32_16x16x128_f8f6f4 v[96:99], v[2:9], v[220:227], v[96:99], v186, v187 op_sel_hi:[0,0,0]
	v_mfma_scale_f32_16x16x128_f8f6f4 v[92:95], v[196:203], v[220:227], v[92:95], v186, v187 op_sel_hi:[0,0,0]
	v_mfma_scale_f32_16x16x128_f8f6f4 v[80:83], v[2:9], v[228:235], v[80:83], v186, v187 op_sel_hi:[0,0,0]
	v_mfma_scale_f32_16x16x128_f8f6f4 v[76:79], v[196:203], v[228:235], v[76:79], v186, v187 op_sel_hi:[0,0,0]
	s_setprio 0
	s_barrier
	s_add_i32 s0, s11, s8
	v_lshl_add_u64 v[160:161], v[160:161], 0, s[26:27]
	s_mov_b32 m0, s0
	ds_read_b128 v[204:207], v185 offset:49152
	ds_read_b128 v[208:211], v185 offset:50176
	ds_read_b128 v[212:215], v185 offset:51200
	ds_read_b128 v[216:219], v185 offset:52224
	ds_read_b128 v[220:223], v185 offset:53248
	ds_read_b128 v[224:227], v185 offset:54272
	ds_read_b128 v[228:231], v185 offset:55296
	ds_read_b128 v[232:235], v185 offset:56320
	global_load_lds_dwordx4 v[160:161], off
	v_lshl_add_u64 v[160:161], v[162:163], 0, s[26:27]
	s_add_i32 m0, s0, 0x2000
	s_add_i32 s0, s28, s8
	global_load_lds_dwordx4 v[160:161], off
	v_lshl_add_u64 v[160:161], v[164:165], 0, s[26:27]
	s_mov_b32 m0, s0
	s_nop 0
	global_load_lds_dwordx4 v[160:161], off
	v_lshl_add_u64 v[160:161], v[166:167], 0, s[26:27]
	s_add_i32 m0, s0, 0x2000
	s_nop 0
	global_load_lds_dwordx4 v[160:161], off
	v_lshl_add_u64 v[160:161], v[168:169], 0, s[26:27]
	s_mov_b32 m0, s62
	s_nop 0
	global_load_lds_dwordx4 v[160:161], off
	v_lshl_add_u64 v[160:161], v[170:171], 0, s[26:27]
	s_mov_b32 m0, s63
	s_nop 0
	global_load_lds_dwordx4 v[160:161], off
	s_waitcnt vmcnt(8)
	s_waitcnt lgkmcnt(0)
	s_barrier
	s_setprio 1
	s_waitcnt lgkmcnt(0)
	v_mfma_scale_f32_16x16x128_f8f6f4 v[72:75], v[172:179], v[204:211], v[72:75], v186, v187 op_sel_hi:[0,0,0]
	v_mfma_scale_f32_16x16x128_f8f6f4 v[68:71], v[188:195], v[204:211], v[68:71], v186, v187 op_sel_hi:[0,0,0]
	v_mfma_scale_f32_16x16x128_f8f6f4 v[56:59], v[172:179], v[212:219], v[56:59], v186, v187 op_sel_hi:[0,0,0]
	v_mfma_scale_f32_16x16x128_f8f6f4 v[52:55], v[188:195], v[212:219], v[52:55], v186, v187 op_sel_hi:[0,0,0]
	v_mfma_scale_f32_16x16x128_f8f6f4 v[40:43], v[172:179], v[220:227], v[40:43], v186, v187 op_sel_hi:[0,0,0]
	v_mfma_scale_f32_16x16x128_f8f6f4 v[36:39], v[188:195], v[220:227], v[36:39], v186, v187 op_sel_hi:[0,0,0]
	v_mfma_scale_f32_16x16x128_f8f6f4 v[24:27], v[172:179], v[228:235], v[24:27], v186, v187 op_sel_hi:[0,0,0]
	v_mfma_scale_f32_16x16x128_f8f6f4 v[20:23], v[188:195], v[228:235], v[20:23], v186, v187 op_sel_hi:[0,0,0]
	v_mfma_scale_f32_16x16x128_f8f6f4 v[64:67], v[2:9], v[204:211], v[64:67], v186, v187 op_sel_hi:[0,0,0]
	v_mfma_scale_f32_16x16x128_f8f6f4 v[60:63], v[196:203], v[204:211], v[60:63], v186, v187 op_sel_hi:[0,0,0]
	v_mfma_scale_f32_16x16x128_f8f6f4 v[48:51], v[2:9], v[212:219], v[48:51], v186, v187 op_sel_hi:[0,0,0]
	v_mfma_scale_f32_16x16x128_f8f6f4 v[44:47], v[196:203], v[212:219], v[44:47], v186, v187 op_sel_hi:[0,0,0]
	v_mfma_scale_f32_16x16x128_f8f6f4 v[32:35], v[2:9], v[220:227], v[32:35], v186, v187 op_sel_hi:[0,0,0]
	v_mfma_scale_f32_16x16x128_f8f6f4 v[28:31], v[196:203], v[220:227], v[28:31], v186, v187 op_sel_hi:[0,0,0]
	v_mfma_scale_f32_16x16x128_f8f6f4 v[16:19], v[2:9], v[228:235], v[16:19], v186, v187 op_sel_hi:[0,0,0]
	v_mfma_scale_f32_16x16x128_f8f6f4 v[12:15], v[196:203], v[228:235], v[12:15], v186, v187 op_sel_hi:[0,0,0]
	s_setprio 0
	s_barrier
	s_add_u32 s64, s64, 0x100
	s_addc_u32 s65, s65, 0
	s_cmp_ge_i32 s10, s68
	s_mov_b32 s0, s10
	s_cbranch_scc1 .LBB0_893

.LBB0_970:
	ds_read_b128 v[18:21], v193
	ds_read_b128 v[22:25], v193 offset:1024
	ds_read_b128 v[26:29], v193 offset:2048
	ds_read_b128 v[30:33], v193 offset:3072
	ds_read_b128 v[2:5], v194
	ds_read_b128 v[6:9], v194 offset:1024
	ds_read_b128 v[10:13], v194 offset:2048
	ds_read_b128 v[14:17], v194 offset:3072
	s_add_i32 s30, s28, 2
	s_add_u32 s31, s0, 0x80
	s_addc_u32 s29, s1, 0
	s_cmp_eq_u32 s68, s28
	s_cselect_b32 s28, s4, s31
	s_cselect_b32 s29, s5, s29
	s_cselect_b32 s45, s37, s11
	s_cselect_b32 s44, s36, s10
	v_lshl_add_u64 v[186:187], s[0:1], 0, v[170:171]
	s_add_i32 m0, s52, 0xc000
	ds_read_b128 v[178:181], v195
	ds_read_b128 v[182:185], v195 offset:1024
	ds_read_b128 v[198:201], v195 offset:2048
	ds_read_b128 v[202:205], v195 offset:3072
	ds_read_b128 v[206:209], v195 offset:4096
	ds_read_b128 v[210:213], v195 offset:5120
	ds_read_b128 v[214:217], v195 offset:6144
	ds_read_b128 v[218:221], v195 offset:7168
	global_load_lds_dwordx4 v[186:187], off
	v_lshl_add_u64 v[186:187], s[0:1], 0, v[172:173]
	s_add_i32 m0, s52, 0xe000
	s_nop 0
	global_load_lds_dwordx4 v[186:187], off
	s_waitcnt vmcnt(8)
	s_waitcnt lgkmcnt(0)
	s_barrier
	s_setprio 1
	s_waitcnt lgkmcnt(0)
	v_mfma_scale_f32_16x16x128_f8f6f4 v[158:161], v[18:25], v[178:185], v[158:161], v196, v197 op_sel_hi:[0,0,0]
	v_mfma_scale_f32_16x16x128_f8f6f4 v[154:157], v[26:33], v[178:185], v[154:157], v196, v197 op_sel_hi:[0,0,0]
	v_mfma_scale_f32_16x16x128_f8f6f4 v[142:145], v[18:25], v[198:205], v[142:145], v196, v197 op_sel_hi:[0,0,0]
	v_mfma_scale_f32_16x16x128_f8f6f4 v[138:141], v[26:33], v[198:205], v[138:141], v196, v197 op_sel_hi:[0,0,0]
	v_mfma_scale_f32_16x16x128_f8f6f4 v[126:129], v[18:25], v[206:213], v[126:129], v196, v197 op_sel_hi:[0,0,0]
	v_mfma_scale_f32_16x16x128_f8f6f4 v[122:125], v[26:33], v[206:213], v[122:125], v196, v197 op_sel_hi:[0,0,0]
	v_mfma_scale_f32_16x16x128_f8f6f4 v[110:113], v[18:25], v[214:221], v[110:113], v196, v197 op_sel_hi:[0,0,0]
	v_mfma_scale_f32_16x16x128_f8f6f4 v[106:109], v[26:33], v[214:221], v[106:109], v196, v197 op_sel_hi:[0,0,0]
	v_mfma_scale_f32_16x16x128_f8f6f4 v[150:153], v[2:9], v[178:185], v[150:153], v196, v197 op_sel_hi:[0,0,0]
	v_mfma_scale_f32_16x16x128_f8f6f4 v[146:149], v[10:17], v[178:185], v[146:149], v196, v197 op_sel_hi:[0,0,0]
	v_mfma_scale_f32_16x16x128_f8f6f4 v[134:137], v[2:9], v[198:205], v[134:137], v196, v197 op_sel_hi:[0,0,0]
	v_mfma_scale_f32_16x16x128_f8f6f4 v[130:133], v[10:17], v[198:205], v[130:133], v196, v197 op_sel_hi:[0,0,0]
	v_mfma_scale_f32_16x16x128_f8f6f4 v[118:121], v[2:9], v[206:213], v[118:121], v196, v197 op_sel_hi:[0,0,0]
	v_mfma_scale_f32_16x16x128_f8f6f4 v[114:117], v[10:17], v[206:213], v[114:117], v196, v197 op_sel_hi:[0,0,0]
	v_mfma_scale_f32_16x16x128_f8f6f4 v[102:105], v[2:9], v[214:221], v[102:105], v196, v197 op_sel_hi:[0,0,0]
	v_mfma_scale_f32_16x16x128_f8f6f4 v[98:101], v[10:17], v[214:221], v[98:101], v196, v197 op_sel_hi:[0,0,0]
	s_setprio 0
	s_barrier
	s_add_i32 s31, s69, s35
	v_lshl_add_u64 v[178:179], s[44:45], 0, v[166:167]
	s_mov_b32 m0, s31
	ds_read_b128 v[198:201], v195 offset:16384
	ds_read_b128 v[202:205], v195 offset:17408
	ds_read_b128 v[206:209], v195 offset:18432
	ds_read_b128 v[210:213], v195 offset:19456
	ds_read_b128 v[214:217], v195 offset:20480
	ds_read_b128 v[218:221], v195 offset:21504
	ds_read_b128 v[222:225], v195 offset:22528
	ds_read_b128 v[226:229], v195 offset:23552
	global_load_lds_dwordx4 v[178:179], off
	s_add_i32 m0, s31, 0x2000
	v_lshl_add_u64 v[180:181], s[44:45], 0, v[162:163]
	s_add_u32 s44, s44, s48
	s_addc_u32 s45, s45, 0
	s_add_i32 s31, s70, s35
	global_load_lds_dwordx4 v[180:181], off
	v_lshl_add_u64 v[182:183], s[44:45], 0, v[166:167]
	s_mov_b32 m0, s31
	v_lshl_add_u64 v[184:185], s[44:45], 0, v[162:163]
	global_load_lds_dwordx4 v[182:183], off
	s_add_i32 m0, s31, 0x2000
	v_lshl_add_u64 v[186:187], s[28:29], 0, v[168:169]
	global_load_lds_dwordx4 v[184:185], off
	s_mov_b32 m0, s52
	v_lshl_add_u64 v[188:189], s[28:29], 0, v[164:165]
	global_load_lds_dwordx4 v[186:187], off
	s_mov_b32 m0, s53
	s_nop 0
	global_load_lds_dwordx4 v[188:189], off
	s_waitcnt vmcnt(8)
	s_waitcnt lgkmcnt(0)
	s_barrier
	s_setprio 1
	s_waitcnt lgkmcnt(0)
	v_mfma_scale_f32_16x16x128_f8f6f4 v[94:97], v[18:25], v[198:205], v[94:97], v196, v197 op_sel_hi:[0,0,0]
	v_mfma_scale_f32_16x16x128_f8f6f4 v[90:93], v[26:33], v[198:205], v[90:93], v196, v197 op_sel_hi:[0,0,0]
	v_mfma_scale_f32_16x16x128_f8f6f4 v[78:81], v[18:25], v[206:213], v[78:81], v196, v197 op_sel_hi:[0,0,0]
	v_mfma_scale_f32_16x16x128_f8f6f4 v[74:77], v[26:33], v[206:213], v[74:77], v196, v197 op_sel_hi:[0,0,0]
	v_mfma_scale_f32_16x16x128_f8f6f4 v[62:65], v[18:25], v[214:221], v[62:65], v196, v197 op_sel_hi:[0,0,0]
	v_mfma_scale_f32_16x16x128_f8f6f4 v[58:61], v[26:33], v[214:221], v[58:61], v196, v197 op_sel_hi:[0,0,0]
	v_mfma_scale_f32_16x16x128_f8f6f4 v[46:49], v[18:25], v[222:229], v[46:49], v196, v197 op_sel_hi:[0,0,0]
	v_mfma_scale_f32_16x16x128_f8f6f4 v[42:45], v[26:33], v[222:229], v[42:45], v196, v197 op_sel_hi:[0,0,0]
	v_mfma_scale_f32_16x16x128_f8f6f4 v[86:89], v[2:9], v[198:205], v[86:89], v196, v197 op_sel_hi:[0,0,0]
	v_mfma_scale_f32_16x16x128_f8f6f4 v[82:85], v[10:17], v[198:205], v[82:85], v196, v197 op_sel_hi:[0,0,0]
	v_mfma_scale_f32_16x16x128_f8f6f4 v[70:73], v[2:9], v[206:213], v[70:73], v196, v197 op_sel_hi:[0,0,0]
	v_mfma_scale_f32_16x16x128_f8f6f4 v[66:69], v[10:17], v[206:213], v[66:69], v196, v197 op_sel_hi:[0,0,0]
	v_mfma_scale_f32_16x16x128_f8f6f4 v[54:57], v[2:9], v[214:221], v[54:57], v196, v197 op_sel_hi:[0,0,0]
	v_mfma_scale_f32_16x16x128_f8f6f4 v[50:53], v[10:17], v[214:221], v[50:53], v196, v197 op_sel_hi:[0,0,0]
	v_mfma_scale_f32_16x16x128_f8f6f4 v[38:41], v[2:9], v[222:229], v[38:41], v196, v197 op_sel_hi:[0,0,0]
	v_mfma_scale_f32_16x16x128_f8f6f4 v[34:37], v[10:17], v[222:229], v[34:37], v196, v197 op_sel_hi:[0,0,0]
	s_setprio 0
	s_barrier
	s_add_i32 s31, 0, 0x18000
	s_add_i32 s44, 0, 0x1c000
	v_add_u32_e32 v14, s31, v191
	v_add_u32_e32 v30, s44, v191
	ds_read_b128 v[2:5], v14
	ds_read_b128 v[6:9], v14 offset:1024
	ds_read_b128 v[10:13], v14 offset:2048
	ds_read_b128 v[14:17], v14 offset:3072
	ds_read_b128 v[18:21], v30
	ds_read_b128 v[22:25], v30 offset:1024
	ds_read_b128 v[26:29], v30 offset:2048
	ds_read_b128 v[30:33], v30 offset:3072
	s_add_u32 s28, s28, s14
	s_addc_u32 s29, s29, s15
	s_mov_b32 m0, s60
	v_lshl_add_u64 v[230:231], s[28:29], 0, v[168:169]
	ds_read_b128 v[198:201], v195 offset:32768
	ds_read_b128 v[202:205], v195 offset:33792
	ds_read_b128 v[206:209], v195 offset:34816
	ds_read_b128 v[210:213], v195 offset:35840
	ds_read_b128 v[214:217], v195 offset:36864
	ds_read_b128 v[218:221], v195 offset:37888
	ds_read_b128 v[222:225], v195 offset:38912
	ds_read_b128 v[226:229], v195 offset:39936
	global_load_lds_dwordx4 v[230:231], off
	v_lshl_add_u64 v[230:231], s[28:29], 0, v[164:165]
	s_mov_b32 m0, s61
	s_nop 0
	global_load_lds_dwordx4 v[230:231], off
	s_waitcnt vmcnt(8)
	s_waitcnt lgkmcnt(0)
	s_barrier
	s_setprio 1
	s_waitcnt lgkmcnt(0)
	v_mfma_scale_f32_16x16x128_f8f6f4 v[158:161], v[2:9], v[198:205], v[158:161], v196, v197 op_sel_hi:[0,0,0]
	v_mfma_scale_f32_16x16x128_f8f6f4 v[154:157], v[10:17], v[198:205], v[154:157], v196, v197 op_sel_hi:[0,0,0]
	v_mfma_scale_f32_16x16x128_f8f6f4 v[142:145], v[2:9], v[206:213], v[142:145], v196, v197 op_sel_hi:[0,0,0]
	v_mfma_scale_f32_16x16x128_f8f6f4 v[138:141], v[10:17], v[206:213], v[138:141], v196, v197 op_sel_hi:[0,0,0]
	v_mfma_scale_f32_16x16x128_f8f6f4 v[126:129], v[2:9], v[214:221], v[126:129], v196, v197 op_sel_hi:[0,0,0]
	v_mfma_scale_f32_16x16x128_f8f6f4 v[122:125], v[10:17], v[214:221], v[122:125], v196, v197 op_sel_hi:[0,0,0]
	v_mfma_scale_f32_16x16x128_f8f6f4 v[110:113], v[2:9], v[222:229], v[110:113], v196, v197 op_sel_hi:[0,0,0]
	v_mfma_scale_f32_16x16x128_f8f6f4 v[106:109], v[10:17], v[222:229], v[106:109], v196, v197 op_sel_hi:[0,0,0]
	v_mfma_scale_f32_16x16x128_f8f6f4 v[150:153], v[18:25], v[198:205], v[150:153], v196, v197 op_sel_hi:[0,0,0]
	v_mfma_scale_f32_16x16x128_f8f6f4 v[146:149], v[26:33], v[198:205], v[146:149], v196, v197 op_sel_hi:[0,0,0]
	v_mfma_scale_f32_16x16x128_f8f6f4 v[134:137], v[18:25], v[206:213], v[134:137], v196, v197 op_sel_hi:[0,0,0]
	v_mfma_scale_f32_16x16x128_f8f6f4 v[130:133], v[26:33], v[206:213], v[130:133], v196, v197 op_sel_hi:[0,0,0]
	v_mfma_scale_f32_16x16x128_f8f6f4 v[118:121], v[18:25], v[214:221], v[118:121], v196, v197 op_sel_hi:[0,0,0]
	v_mfma_scale_f32_16x16x128_f8f6f4 v[114:117], v[26:33], v[214:221], v[114:117], v196, v197 op_sel_hi:[0,0,0]
	v_mfma_scale_f32_16x16x128_f8f6f4 v[102:105], v[18:25], v[222:229], v[102:105], v196, v197 op_sel_hi:[0,0,0]
	v_mfma_scale_f32_16x16x128_f8f6f4 v[98:101], v[26:33], v[222:229], v[98:101], v196, v197 op_sel_hi:[0,0,0]
	s_setprio 0
	s_barrier
	s_add_i32 s28, s31, s35
	v_lshl_add_u64 v[178:179], v[178:179], 0, s[22:23]
	s_mov_b32 m0, s28
	ds_read_b128 v[198:201], v195 offset:49152
	ds_read_b128 v[202:205], v195 offset:50176
	ds_read_b128 v[206:209], v195 offset:51200
	ds_read_b128 v[210:213], v195 offset:52224
	ds_read_b128 v[214:217], v195 offset:53248
	ds_read_b128 v[218:221], v195 offset:54272
	ds_read_b128 v[222:225], v195 offset:55296
	ds_read_b128 v[226:229], v195 offset:56320
	global_load_lds_dwordx4 v[178:179], off
	v_lshl_add_u64 v[178:179], v[180:181], 0, s[22:23]
	s_add_i32 m0, s28, 0x2000
	s_add_i32 s28, s44, s35
	global_load_lds_dwordx4 v[178:179], off
	v_lshl_add_u64 v[178:179], v[182:183], 0, s[22:23]
	s_mov_b32 m0, s28
	s_nop 0
	global_load_lds_dwordx4 v[178:179], off
	v_lshl_add_u64 v[178:179], v[184:185], 0, s[22:23]
	s_add_i32 m0, s28, 0x2000
	s_nop 0
	global_load_lds_dwordx4 v[178:179], off
	v_lshl_add_u64 v[178:179], v[186:187], 0, s[22:23]
	s_mov_b32 m0, s63
	s_nop 0
	global_load_lds_dwordx4 v[178:179], off
	v_lshl_add_u64 v[178:179], v[188:189], 0, s[22:23]
	s_mov_b32 m0, s64
	s_nop 0
	global_load_lds_dwordx4 v[178:179], off
	s_waitcnt vmcnt(8)
	s_waitcnt lgkmcnt(0)
	s_barrier
	s_setprio 1
	s_waitcnt lgkmcnt(0)
	v_mfma_scale_f32_16x16x128_f8f6f4 v[94:97], v[2:9], v[198:205], v[94:97], v196, v197 op_sel_hi:[0,0,0]
	v_mfma_scale_f32_16x16x128_f8f6f4 v[90:93], v[10:17], v[198:205], v[90:93], v196, v197 op_sel_hi:[0,0,0]
	v_mfma_scale_f32_16x16x128_f8f6f4 v[78:81], v[2:9], v[206:213], v[78:81], v196, v197 op_sel_hi:[0,0,0]
	v_mfma_scale_f32_16x16x128_f8f6f4 v[74:77], v[10:17], v[206:213], v[74:77], v196, v197 op_sel_hi:[0,0,0]
	v_mfma_scale_f32_16x16x128_f8f6f4 v[62:65], v[2:9], v[214:221], v[62:65], v196, v197 op_sel_hi:[0,0,0]
	v_mfma_scale_f32_16x16x128_f8f6f4 v[58:61], v[10:17], v[214:221], v[58:61], v196, v197 op_sel_hi:[0,0,0]
	v_mfma_scale_f32_16x16x128_f8f6f4 v[46:49], v[2:9], v[222:229], v[46:49], v196, v197 op_sel_hi:[0,0,0]
	v_mfma_scale_f32_16x16x128_f8f6f4 v[42:45], v[10:17], v[222:229], v[42:45], v196, v197 op_sel_hi:[0,0,0]
	v_mfma_scale_f32_16x16x128_f8f6f4 v[86:89], v[18:25], v[198:205], v[86:89], v196, v197 op_sel_hi:[0,0,0]
	v_mfma_scale_f32_16x16x128_f8f6f4 v[82:85], v[26:33], v[198:205], v[82:85], v196, v197 op_sel_hi:[0,0,0]
	v_mfma_scale_f32_16x16x128_f8f6f4 v[70:73], v[18:25], v[206:213], v[70:73], v196, v197 op_sel_hi:[0,0,0]
	v_mfma_scale_f32_16x16x128_f8f6f4 v[66:69], v[26:33], v[206:213], v[66:69], v196, v197 op_sel_hi:[0,0,0]
	v_mfma_scale_f32_16x16x128_f8f6f4 v[54:57], v[18:25], v[214:221], v[54:57], v196, v197 op_sel_hi:[0,0,0]
	v_mfma_scale_f32_16x16x128_f8f6f4 v[50:53], v[26:33], v[214:221], v[50:53], v196, v197 op_sel_hi:[0,0,0]
	v_mfma_scale_f32_16x16x128_f8f6f4 v[38:41], v[18:25], v[222:229], v[38:41], v196, v197 op_sel_hi:[0,0,0]
	v_mfma_scale_f32_16x16x128_f8f6f4 v[34:37], v[26:33], v[222:229], v[34:37], v196, v197 op_sel_hi:[0,0,0]
	s_setprio 0
	s_barrier
	s_add_u32 s0, s0, 0x100
	s_addc_u32 s1, s1, 0
	s_add_u32 s10, s10, 0x100
	s_addc_u32 s11, s11, 0
	s_cmp_ge_i32 s30, s65
	s_mov_b32 s28, s30
	s_cbranch_scc0 .LBB0_970

.LBB0_1216:
	s_add_i32 s65, s65, 2
	s_add_u32 s60, s78, 0x100
	v_add_u32_e32 v2, s97, v157
	s_addc_u32 s61, s79, 0
	ds_read_b128 v[186:189], v2
	ds_read_b128 v[190:193], v2 offset:1024
	ds_read_b128 v[194:197], v2 offset:2048
	ds_read_b128 v[198:201], v2 offset:3072
	v_add_u32_e32 v2, s8, v157
	s_and_b64 s[62:63], s[6:7], exec
	ds_read_b128 v[202:205], v2
	ds_read_b128 v[206:209], v2 offset:1024
	ds_read_b128 v[210:213], v2 offset:2048
	ds_read_b128 v[214:217], v2 offset:3072
	s_cselect_b32 s62, 0, s60
	s_cselect_b32 s63, 0, s61
	s_add_u32 s62, s48, s62
	s_addc_u32 s63, s49, s63
	s_add_u32 s71, s22, s78
	s_addc_u32 vcc_lo, s31, s79
	s_and_b64 s[80:81], s[6:7], exec
	s_cselect_b32 s81, s77, vcc_lo
	s_cselect_b32 s80, s76, s71
	v_cndmask_b32_e64 v2, v184, v156, s[6:7]
	v_cndmask_b32_e64 v166, v185, v158, s[6:7]
	v_cndmask_b32_e64 v5, v4, v177, s[6:7]
	v_cndmask_b32_e64 v151, v162, v178, s[6:7]
	v_lshl_add_u64 v[140:141], v[136:137], 0, s[78:79]
	s_add_i32 m0, s84, 0xc000
	ds_read_b128 v[218:221], v159
	ds_read_b128 v[222:225], v159 offset:1024
	ds_read_b128 v[226:229], v159 offset:2048
	ds_read_b128 v[230:233], v159 offset:3072
	ds_read_b128 v[234:237], v159 offset:4096
	ds_read_b128 v[238:241], v159 offset:5120
	ds_read_b128 v[242:245], v159 offset:6144
	ds_read_b128 v[246:249], v159 offset:7168
	global_load_lds_dwordx4 v[140:141], off
	v_lshl_add_u64 v[140:141], v[138:139], 0, s[78:79]
	s_add_i32 m0, s84, 0xe000
	s_nop 0
	global_load_lds_dwordx4 v[140:141], off
	s_waitcnt vmcnt(8)
	s_waitcnt lgkmcnt(0)
	s_barrier
	s_setprio 1
	s_waitcnt lgkmcnt(0)
	v_mfma_scale_f32_16x16x128_f8f6f4 v[130:133], v[186:193], v[218:225], v[130:133], v181, v182 op_sel_hi:[0,0,0]
	v_mfma_scale_f32_16x16x128_f8f6f4 v[126:129], v[194:201], v[218:225], v[126:129], v181, v182 op_sel_hi:[0,0,0]
	v_mfma_scale_f32_16x16x128_f8f6f4 v[122:125], v[186:193], v[226:233], v[122:125], v181, v182 op_sel_hi:[0,0,0]
	v_mfma_scale_f32_16x16x128_f8f6f4 v[118:121], v[194:201], v[226:233], v[118:121], v181, v182 op_sel_hi:[0,0,0]
	v_mfma_scale_f32_16x16x128_f8f6f4 v[114:117], v[186:193], v[234:241], v[114:117], v181, v182 op_sel_hi:[0,0,0]
	v_mfma_scale_f32_16x16x128_f8f6f4 v[110:113], v[194:201], v[234:241], v[110:113], v181, v182 op_sel_hi:[0,0,0]
	v_mfma_scale_f32_16x16x128_f8f6f4 v[106:109], v[186:193], v[242:249], v[106:109], v181, v182 op_sel_hi:[0,0,0]
	v_mfma_scale_f32_16x16x128_f8f6f4 v[102:105], v[194:201], v[242:249], v[102:105], v181, v182 op_sel_hi:[0,0,0]
	v_mfma_scale_f32_16x16x128_f8f6f4 v[98:101], v[202:209], v[218:225], v[98:101], v181, v182 op_sel_hi:[0,0,0]
	v_mfma_scale_f32_16x16x128_f8f6f4 v[94:97], v[210:217], v[218:225], v[94:97], v181, v182 op_sel_hi:[0,0,0]
	v_mfma_scale_f32_16x16x128_f8f6f4 v[90:93], v[202:209], v[226:233], v[90:93], v181, v182 op_sel_hi:[0,0,0]
	v_mfma_scale_f32_16x16x128_f8f6f4 v[86:89], v[210:217], v[226:233], v[86:89], v181, v182 op_sel_hi:[0,0,0]
	v_mfma_scale_f32_16x16x128_f8f6f4 v[82:85], v[202:209], v[234:241], v[82:85], v181, v182 op_sel_hi:[0,0,0]
	v_mfma_scale_f32_16x16x128_f8f6f4 v[78:81], v[210:217], v[234:241], v[78:81], v181, v182 op_sel_hi:[0,0,0]
	v_mfma_scale_f32_16x16x128_f8f6f4 v[74:77], v[202:209], v[242:249], v[74:77], v181, v182 op_sel_hi:[0,0,0]
	v_mfma_scale_f32_16x16x128_f8f6f4 v[70:73], v[210:217], v[242:249], v[70:73], v181, v182 op_sel_hi:[0,0,0]
	s_setprio 0
	s_barrier
	s_add_i32 s6, s97, s83
	v_lshl_add_u64 v[140:141], s[80:81], 0, v[148:149]
	s_mov_b32 m0, s6
	ds_read_b128 v[218:221], v159 offset:16384
	ds_read_b128 v[222:225], v159 offset:17408
	ds_read_b128 v[226:229], v159 offset:18432
	ds_read_b128 v[230:233], v159 offset:19456
	ds_read_b128 v[234:237], v159 offset:20480
	ds_read_b128 v[238:241], v159 offset:21504
	ds_read_b128 v[242:245], v159 offset:22528
	ds_read_b128 v[246:249], v159 offset:23552
	global_load_lds_dwordx4 v[140:141], off
	s_add_i32 m0, s6, 0x2000
	s_add_u32 s6, s80, s51
	v_lshl_add_u64 v[142:143], s[80:81], 0, v[160:161]
	s_addc_u32 s7, s81, 0
	s_add_i32 s71, s8, s83
	global_load_lds_dwordx4 v[142:143], off
	v_lshl_add_u64 v[144:145], s[6:7], 0, v[148:149]
	s_mov_b32 m0, s71
	v_lshl_add_u64 v[164:165], s[6:7], 0, v[160:161]
	global_load_lds_dwordx4 v[144:145], off
	s_add_i32 m0, s71, 0x2000
	v_mov_b32_e32 v167, v3
	global_load_lds_dwordx4 v[164:165], off
	s_mov_b32 m0, s84
	v_lshl_add_u64 v[168:169], s[62:63], 0, v[2:3]
	global_load_lds_dwordx4 v2, s[62:63]
	s_mov_b32 m0, s85
	s_nop 0
	global_load_lds_dwordx4 v166, s[62:63]
	s_waitcnt vmcnt(8)
	s_waitcnt lgkmcnt(0)
	v_lshl_add_u64 v[166:167], s[62:63], 0, v[166:167]
	s_barrier
	s_setprio 1
	s_waitcnt lgkmcnt(0)
	v_mfma_scale_f32_16x16x128_f8f6f4 v[66:69], v[186:193], v[218:225], v[66:69], v181, v182 op_sel_hi:[0,0,0]
	v_mfma_scale_f32_16x16x128_f8f6f4 v[62:65], v[194:201], v[218:225], v[62:65], v181, v182 op_sel_hi:[0,0,0]
	v_mfma_scale_f32_16x16x128_f8f6f4 v[58:61], v[186:193], v[226:233], v[58:61], v181, v182 op_sel_hi:[0,0,0]
	v_mfma_scale_f32_16x16x128_f8f6f4 v[54:57], v[194:201], v[226:233], v[54:57], v181, v182 op_sel_hi:[0,0,0]
	v_mfma_scale_f32_16x16x128_f8f6f4 v[50:53], v[186:193], v[234:241], v[50:53], v181, v182 op_sel_hi:[0,0,0]
	v_mfma_scale_f32_16x16x128_f8f6f4 v[46:49], v[194:201], v[234:241], v[46:49], v181, v182 op_sel_hi:[0,0,0]
	v_mfma_scale_f32_16x16x128_f8f6f4 v[42:45], v[186:193], v[242:249], v[42:45], v181, v182 op_sel_hi:[0,0,0]
	v_mfma_scale_f32_16x16x128_f8f6f4 v[38:41], v[194:201], v[242:249], v[38:41], v181, v182 op_sel_hi:[0,0,0]
	v_mfma_scale_f32_16x16x128_f8f6f4 v[34:37], v[202:209], v[218:225], v[34:37], v181, v182 op_sel_hi:[0,0,0]
	v_mfma_scale_f32_16x16x128_f8f6f4 v[30:33], v[210:217], v[218:225], v[30:33], v181, v182 op_sel_hi:[0,0,0]
	v_mfma_scale_f32_16x16x128_f8f6f4 v[26:29], v[202:209], v[226:233], v[26:29], v181, v182 op_sel_hi:[0,0,0]
	v_mfma_scale_f32_16x16x128_f8f6f4 v[22:25], v[210:217], v[226:233], v[22:25], v181, v182 op_sel_hi:[0,0,0]
	v_mfma_scale_f32_16x16x128_f8f6f4 v[18:21], v[202:209], v[234:241], v[18:21], v181, v182 op_sel_hi:[0,0,0]
	v_mfma_scale_f32_16x16x128_f8f6f4 v[14:17], v[210:217], v[234:241], v[14:17], v181, v182 op_sel_hi:[0,0,0]
	v_mfma_scale_f32_16x16x128_f8f6f4 v[10:13], v[202:209], v[242:249], v[10:13], v181, v182 op_sel_hi:[0,0,0]
	v_mfma_scale_f32_16x16x128_f8f6f4 v[6:9], v[210:217], v[242:249], v[6:9], v181, v182 op_sel_hi:[0,0,0]
	s_setprio 0
	s_barrier
	s_add_i32 s6, 0, 0x18000
	v_add_u32_e32 v2, s6, v157
	s_add_i32 s7, 0, 0x1c000
	ds_read_b128 v[186:189], v2
	ds_read_b128 v[190:193], v2 offset:1024
	ds_read_b128 v[194:197], v2 offset:2048
	ds_read_b128 v[198:201], v2 offset:3072
	v_add_u32_e32 v2, s7, v157
	ds_read_b128 v[202:205], v2
	ds_read_b128 v[206:209], v2 offset:1024
	ds_read_b128 v[210:213], v2 offset:2048
	ds_read_b128 v[214:217], v2 offset:3072
	s_mov_b32 m0, s86
	ds_read_b128 v[218:221], v159 offset:32768
	ds_read_b128 v[222:225], v159 offset:33792
	ds_read_b128 v[226:229], v159 offset:34816
	ds_read_b128 v[230:233], v159 offset:35840
	ds_read_b128 v[234:237], v159 offset:36864
	ds_read_b128 v[238:241], v159 offset:37888
	ds_read_b128 v[242:245], v159 offset:38912
	ds_read_b128 v[246:249], v159 offset:39936
	global_load_lds_dwordx4 v5, s[62:63]
	s_mov_b32 m0, s87
	s_nop 0
	global_load_lds_dwordx4 v151, s[62:63]
	s_waitcnt vmcnt(8)
	s_waitcnt lgkmcnt(0)
	s_barrier
	s_setprio 1
	s_waitcnt lgkmcnt(0)
	v_mfma_scale_f32_16x16x128_f8f6f4 v[130:133], v[186:193], v[218:225], v[130:133], v181, v182 op_sel_hi:[0,0,0]
	v_mfma_scale_f32_16x16x128_f8f6f4 v[126:129], v[194:201], v[218:225], v[126:129], v181, v182 op_sel_hi:[0,0,0]
	v_mfma_scale_f32_16x16x128_f8f6f4 v[122:125], v[186:193], v[226:233], v[122:125], v181, v182 op_sel_hi:[0,0,0]
	v_mfma_scale_f32_16x16x128_f8f6f4 v[118:121], v[194:201], v[226:233], v[118:121], v181, v182 op_sel_hi:[0,0,0]
	v_mfma_scale_f32_16x16x128_f8f6f4 v[114:117], v[186:193], v[234:241], v[114:117], v181, v182 op_sel_hi:[0,0,0]
	v_mfma_scale_f32_16x16x128_f8f6f4 v[110:113], v[194:201], v[234:241], v[110:113], v181, v182 op_sel_hi:[0,0,0]
	v_mfma_scale_f32_16x16x128_f8f6f4 v[106:109], v[186:193], v[242:249], v[106:109], v181, v182 op_sel_hi:[0,0,0]
	v_mfma_scale_f32_16x16x128_f8f6f4 v[102:105], v[194:201], v[242:249], v[102:105], v181, v182 op_sel_hi:[0,0,0]
	v_mfma_scale_f32_16x16x128_f8f6f4 v[98:101], v[202:209], v[218:225], v[98:101], v181, v182 op_sel_hi:[0,0,0]
	v_mfma_scale_f32_16x16x128_f8f6f4 v[94:97], v[210:217], v[218:225], v[94:97], v181, v182 op_sel_hi:[0,0,0]
	v_mfma_scale_f32_16x16x128_f8f6f4 v[90:93], v[202:209], v[226:233], v[90:93], v181, v182 op_sel_hi:[0,0,0]
	v_mfma_scale_f32_16x16x128_f8f6f4 v[86:89], v[210:217], v[226:233], v[86:89], v181, v182 op_sel_hi:[0,0,0]
	v_mfma_scale_f32_16x16x128_f8f6f4 v[82:85], v[202:209], v[234:241], v[82:85], v181, v182 op_sel_hi:[0,0,0]
	v_mfma_scale_f32_16x16x128_f8f6f4 v[78:81], v[210:217], v[234:241], v[78:81], v181, v182 op_sel_hi:[0,0,0]
	v_mfma_scale_f32_16x16x128_f8f6f4 v[74:77], v[202:209], v[242:249], v[74:77], v181, v182 op_sel_hi:[0,0,0]
	v_mfma_scale_f32_16x16x128_f8f6f4 v[70:73], v[210:217], v[242:249], v[70:73], v181, v182 op_sel_hi:[0,0,0]
	s_setprio 0
	s_barrier
	s_add_i32 s6, s6, s83
	v_lshl_add_u64 v[140:141], v[140:141], 0, s[38:39]
	s_mov_b32 m0, s6
	ds_read_b128 v[218:221], v159 offset:49152
	ds_read_b128 v[222:225], v159 offset:50176
	ds_read_b128 v[226:229], v159 offset:51200
	ds_read_b128 v[230:233], v159 offset:52224
	ds_read_b128 v[234:237], v159 offset:53248
	ds_read_b128 v[238:241], v159 offset:54272
	ds_read_b128 v[242:245], v159 offset:55296
	ds_read_b128 v[246:249], v159 offset:56320
	global_load_lds_dwordx4 v[140:141], off
	v_lshl_add_u64 v[140:141], v[142:143], 0, s[38:39]
	s_add_i32 m0, s6, 0x2000
	s_add_i32 s6, s7, s83
	global_load_lds_dwordx4 v[140:141], off
	v_lshl_add_u64 v[140:141], v[144:145], 0, s[38:39]
	s_mov_b32 m0, s6
	s_nop 0
	global_load_lds_dwordx4 v[140:141], off
	v_lshl_add_u64 v[140:141], v[164:165], 0, s[38:39]
	s_add_i32 m0, s6, 0x2000
	s_nop 0
	global_load_lds_dwordx4 v[140:141], off
	v_lshl_add_u64 v[140:141], v[168:169], 0, s[38:39]
	s_mov_b32 m0, s90
	s_nop 0
	global_load_lds_dwordx4 v[140:141], off
	v_lshl_add_u64 v[140:141], v[166:167], 0, s[38:39]
	s_mov_b32 m0, s91
	s_nop 0
	global_load_lds_dwordx4 v[140:141], off
	s_waitcnt vmcnt(8)
	s_waitcnt lgkmcnt(0)
	s_barrier
	s_setprio 1
	s_waitcnt lgkmcnt(0)
	v_mfma_scale_f32_16x16x128_f8f6f4 v[66:69], v[186:193], v[218:225], v[66:69], v181, v182 op_sel_hi:[0,0,0]
	v_mfma_scale_f32_16x16x128_f8f6f4 v[62:65], v[194:201], v[218:225], v[62:65], v181, v182 op_sel_hi:[0,0,0]
	v_mfma_scale_f32_16x16x128_f8f6f4 v[58:61], v[186:193], v[226:233], v[58:61], v181, v182 op_sel_hi:[0,0,0]
	v_mfma_scale_f32_16x16x128_f8f6f4 v[54:57], v[194:201], v[226:233], v[54:57], v181, v182 op_sel_hi:[0,0,0]
	v_mfma_scale_f32_16x16x128_f8f6f4 v[50:53], v[186:193], v[234:241], v[50:53], v181, v182 op_sel_hi:[0,0,0]
	v_mfma_scale_f32_16x16x128_f8f6f4 v[46:49], v[194:201], v[234:241], v[46:49], v181, v182 op_sel_hi:[0,0,0]
	v_mfma_scale_f32_16x16x128_f8f6f4 v[42:45], v[186:193], v[242:249], v[42:45], v181, v182 op_sel_hi:[0,0,0]
	v_mfma_scale_f32_16x16x128_f8f6f4 v[38:41], v[194:201], v[242:249], v[38:41], v181, v182 op_sel_hi:[0,0,0]
	v_mfma_scale_f32_16x16x128_f8f6f4 v[34:37], v[202:209], v[218:225], v[34:37], v181, v182 op_sel_hi:[0,0,0]
	v_mfma_scale_f32_16x16x128_f8f6f4 v[30:33], v[210:217], v[218:225], v[30:33], v181, v182 op_sel_hi:[0,0,0]
	v_mfma_scale_f32_16x16x128_f8f6f4 v[26:29], v[202:209], v[226:233], v[26:29], v181, v182 op_sel_hi:[0,0,0]
	v_mfma_scale_f32_16x16x128_f8f6f4 v[22:25], v[210:217], v[226:233], v[22:25], v181, v182 op_sel_hi:[0,0,0]
	v_mfma_scale_f32_16x16x128_f8f6f4 v[18:21], v[202:209], v[234:241], v[18:21], v181, v182 op_sel_hi:[0,0,0]
	v_mfma_scale_f32_16x16x128_f8f6f4 v[14:17], v[210:217], v[234:241], v[14:17], v181, v182 op_sel_hi:[0,0,0]
	v_mfma_scale_f32_16x16x128_f8f6f4 v[10:13], v[202:209], v[242:249], v[10:13], v181, v182 op_sel_hi:[0,0,0]
	v_mfma_scale_f32_16x16x128_f8f6f4 v[6:9], v[210:217], v[242:249], v[6:9], v181, v182 op_sel_hi:[0,0,0]
	s_setprio 0
	s_barrier
	s_cmp_ge_i32 s65, s15
	s_cbranch_scc1 .LBB0_1218
	s_mov_b64 s[78:79], s[60:61]
	s_branch .LBB0_1210

.LBB0_1316:
	v_add_u32_e32 v8, s96, v170
	ds_read_b128 v[0:3], v8
	ds_read_b128 v[4:7], v8 offset:1024
	ds_read_b128 v[178:181], v8 offset:2048
	ds_read_b128 v[182:185], v8 offset:3072
	v_add_u32_e32 v8, s97, v170
	ds_read_b128 v[186:189], v8
	ds_read_b128 v[190:193], v8 offset:1024
	ds_read_b128 v[194:197], v8 offset:2048
	ds_read_b128 v[198:201], v8 offset:3072
	s_add_i32 s47, s47, 2
	s_add_u32 s60, s52, 0x80
	s_addc_u32 s61, s53, 0
	s_and_b64 s[2:3], s[2:3], exec
	s_cselect_b32 s61, s61, s29
	s_cselect_b32 s60, s60, s28
	s_cselect_b32 s3, s31, s49
	s_cselect_b32 s2, s30, s48
	v_lshl_add_u64 v[148:149], s[52:53], 0, v[162:163]
	s_add_i32 m0, s68, 0xc000
	ds_read_b128 v[140:143], v174
	ds_read_b128 v[144:147], v174 offset:1024
	ds_read_b128 v[202:205], v174 offset:2048
	ds_read_b128 v[206:209], v174 offset:3072
	ds_read_b128 v[210:213], v174 offset:4096
	ds_read_b128 v[214:217], v174 offset:5120
	ds_read_b128 v[218:221], v174 offset:6144
	ds_read_b128 v[222:225], v174 offset:7168
	global_load_lds_dwordx4 v[148:149], off
	v_lshl_add_u64 v[148:149], s[52:53], 0, v[164:165]
	s_add_i32 m0, s68, 0xe000
	s_nop 0
	global_load_lds_dwordx4 v[148:149], off
	s_waitcnt vmcnt(8)
	s_waitcnt lgkmcnt(0)
	s_barrier
	s_setprio 1
	s_waitcnt lgkmcnt(0)
	v_mfma_scale_f32_16x16x128_f8f6f4 v[120:123], v[0:7], v[140:147], v[120:123], v175, v176 op_sel_hi:[0,0,0]
	v_mfma_scale_f32_16x16x128_f8f6f4 v[116:119], v[178:185], v[140:147], v[116:119], v175, v176 op_sel_hi:[0,0,0]
	v_mfma_scale_f32_16x16x128_f8f6f4 v[112:115], v[0:7], v[202:209], v[112:115], v175, v176 op_sel_hi:[0,0,0]
	v_mfma_scale_f32_16x16x128_f8f6f4 v[108:111], v[178:185], v[202:209], v[108:111], v175, v176 op_sel_hi:[0,0,0]
	v_mfma_scale_f32_16x16x128_f8f6f4 v[104:107], v[0:7], v[210:217], v[104:107], v175, v176 op_sel_hi:[0,0,0]
	v_mfma_scale_f32_16x16x128_f8f6f4 v[100:103], v[178:185], v[210:217], v[100:103], v175, v176 op_sel_hi:[0,0,0]
	v_mfma_scale_f32_16x16x128_f8f6f4 v[96:99], v[0:7], v[218:225], v[96:99], v175, v176 op_sel_hi:[0,0,0]
	v_mfma_scale_f32_16x16x128_f8f6f4 v[92:95], v[178:185], v[218:225], v[92:95], v175, v176 op_sel_hi:[0,0,0]
	v_mfma_scale_f32_16x16x128_f8f6f4 v[88:91], v[186:193], v[140:147], v[88:91], v175, v176 op_sel_hi:[0,0,0]
	v_mfma_scale_f32_16x16x128_f8f6f4 v[84:87], v[194:201], v[140:147], v[84:87], v175, v176 op_sel_hi:[0,0,0]
	v_mfma_scale_f32_16x16x128_f8f6f4 v[80:83], v[186:193], v[202:209], v[80:83], v175, v176 op_sel_hi:[0,0,0]
	v_mfma_scale_f32_16x16x128_f8f6f4 v[76:79], v[194:201], v[202:209], v[76:79], v175, v176 op_sel_hi:[0,0,0]
	v_mfma_scale_f32_16x16x128_f8f6f4 v[72:75], v[186:193], v[210:217], v[72:75], v175, v176 op_sel_hi:[0,0,0]
	v_mfma_scale_f32_16x16x128_f8f6f4 v[68:71], v[194:201], v[210:217], v[68:71], v175, v176 op_sel_hi:[0,0,0]
	v_mfma_scale_f32_16x16x128_f8f6f4 v[64:67], v[186:193], v[218:225], v[64:67], v175, v176 op_sel_hi:[0,0,0]
	v_mfma_scale_f32_16x16x128_f8f6f4 v[60:63], v[194:201], v[218:225], v[60:63], v175, v176 op_sel_hi:[0,0,0]
	s_setprio 0
	s_barrier
	s_add_i32 vcc_lo, s96, s65
	v_lshl_add_u64 v[140:141], s[2:3], 0, v[152:153]
	s_mov_b32 m0, vcc_lo
	ds_read_b128 v[202:205], v174 offset:16384
	ds_read_b128 v[206:209], v174 offset:17408
	ds_read_b128 v[210:213], v174 offset:18432
	ds_read_b128 v[214:217], v174 offset:19456
	ds_read_b128 v[218:221], v174 offset:20480
	ds_read_b128 v[222:225], v174 offset:21504
	ds_read_b128 v[226:229], v174 offset:22528
	ds_read_b128 v[230:233], v174 offset:23552
	global_load_lds_dwordx4 v[140:141], off
	s_add_i32 m0, vcc_lo, 0x2000
	v_lshl_add_u64 v[142:143], s[2:3], 0, v[160:161]
	s_add_u32 s2, s2, s64
	s_addc_u32 s3, s3, 0
	s_add_i32 vcc_lo, s97, s65
	global_load_lds_dwordx4 v[142:143], off
	v_lshl_add_u64 v[144:145], s[2:3], 0, v[152:153]
	s_mov_b32 m0, vcc_lo
	v_lshl_add_u64 v[146:147], s[2:3], 0, v[160:161]
	global_load_lds_dwordx4 v[144:145], off
	s_add_i32 m0, vcc_lo, 0x2000
	v_lshl_add_u64 v[148:149], s[60:61], 0, v[156:157]
	global_load_lds_dwordx4 v[146:147], off
	s_mov_b32 m0, s68
	v_lshl_add_u64 v[150:151], s[60:61], 0, v[158:159]
	global_load_lds_dwordx4 v[148:149], off
	s_mov_b32 m0, s69
	s_nop 0
	global_load_lds_dwordx4 v[150:151], off
	s_waitcnt vmcnt(8)
	s_waitcnt lgkmcnt(0)
	s_barrier
	s_setprio 1
	s_waitcnt lgkmcnt(0)
	v_mfma_scale_f32_16x16x128_f8f6f4 v[56:59], v[0:7], v[202:209], v[56:59], v175, v176 op_sel_hi:[0,0,0]
	v_mfma_scale_f32_16x16x128_f8f6f4 v[52:55], v[178:185], v[202:209], v[52:55], v175, v176 op_sel_hi:[0,0,0]
	v_mfma_scale_f32_16x16x128_f8f6f4 v[48:51], v[0:7], v[210:217], v[48:51], v175, v176 op_sel_hi:[0,0,0]
	v_mfma_scale_f32_16x16x128_f8f6f4 v[44:47], v[178:185], v[210:217], v[44:47], v175, v176 op_sel_hi:[0,0,0]
	v_mfma_scale_f32_16x16x128_f8f6f4 v[40:43], v[0:7], v[218:225], v[40:43], v175, v176 op_sel_hi:[0,0,0]
	v_mfma_scale_f32_16x16x128_f8f6f4 v[36:39], v[178:185], v[218:225], v[36:39], v175, v176 op_sel_hi:[0,0,0]
	v_mfma_scale_f32_16x16x128_f8f6f4 v[32:35], v[0:7], v[226:233], v[32:35], v175, v176 op_sel_hi:[0,0,0]
	v_mfma_scale_f32_16x16x128_f8f6f4 v[28:31], v[178:185], v[226:233], v[28:31], v175, v176 op_sel_hi:[0,0,0]
	v_mfma_scale_f32_16x16x128_f8f6f4 v[24:27], v[186:193], v[202:209], v[24:27], v175, v176 op_sel_hi:[0,0,0]
	v_mfma_scale_f32_16x16x128_f8f6f4 v[20:23], v[194:201], v[202:209], v[20:23], v175, v176 op_sel_hi:[0,0,0]
	v_mfma_scale_f32_16x16x128_f8f6f4 v[16:19], v[186:193], v[210:217], v[16:19], v175, v176 op_sel_hi:[0,0,0]
	v_mfma_scale_f32_16x16x128_f8f6f4 v[12:15], v[194:201], v[210:217], v[12:15], v175, v176 op_sel_hi:[0,0,0]
	v_mfma_scale_f32_16x16x128_f8f6f4 v[124:127], v[186:193], v[218:225], v[124:127], v175, v176 op_sel_hi:[0,0,0]
	v_mfma_scale_f32_16x16x128_f8f6f4 v[128:131], v[194:201], v[218:225], v[128:131], v175, v176 op_sel_hi:[0,0,0]
	v_mfma_scale_f32_16x16x128_f8f6f4 v[132:135], v[186:193], v[226:233], v[132:135], v175, v176 op_sel_hi:[0,0,0]
	v_mfma_scale_f32_16x16x128_f8f6f4 v[136:139], v[194:201], v[226:233], v[136:139], v175, v176 op_sel_hi:[0,0,0]
	s_setprio 0
	s_barrier
	s_add_i32 s2, 0, 0x18000
	s_add_i32 s3, 0, 0x1c000
	v_add_u32_e32 v0, s2, v170
	v_add_u32_e32 v8, s3, v170
	ds_read_b128 v[178:181], v0
	ds_read_b128 v[182:185], v0 offset:1024
	ds_read_b128 v[186:189], v0 offset:2048
	ds_read_b128 v[190:193], v0 offset:3072
	ds_read_b128 v[0:3], v8
	ds_read_b128 v[4:7], v8 offset:1024
	ds_read_b128 v[194:197], v8 offset:2048
	ds_read_b128 v[198:201], v8 offset:3072
	s_add_u32 s60, s60, s20
	s_addc_u32 s61, s61, s21
	s_mov_b32 m0, s70
	v_lshl_add_u64 v[166:167], s[60:61], 0, v[156:157]
	ds_read_b128 v[202:205], v174 offset:32768
	ds_read_b128 v[206:209], v174 offset:33792
	ds_read_b128 v[210:213], v174 offset:34816
	ds_read_b128 v[214:217], v174 offset:35840
	ds_read_b128 v[218:221], v174 offset:36864
	ds_read_b128 v[222:225], v174 offset:37888
	ds_read_b128 v[226:229], v174 offset:38912
	ds_read_b128 v[230:233], v174 offset:39936
	global_load_lds_dwordx4 v[166:167], off
	v_lshl_add_u64 v[166:167], s[60:61], 0, v[158:159]
	s_mov_b32 m0, s71
	s_nop 0
	global_load_lds_dwordx4 v[166:167], off
	s_waitcnt vmcnt(8)
	s_waitcnt lgkmcnt(0)
	s_barrier
	s_setprio 1
	s_waitcnt lgkmcnt(0)
	v_mfma_scale_f32_16x16x128_f8f6f4 v[120:123], v[178:185], v[202:209], v[120:123], v175, v176 op_sel_hi:[0,0,0]
	v_mfma_scale_f32_16x16x128_f8f6f4 v[116:119], v[186:193], v[202:209], v[116:119], v175, v176 op_sel_hi:[0,0,0]
	v_mfma_scale_f32_16x16x128_f8f6f4 v[112:115], v[178:185], v[210:217], v[112:115], v175, v176 op_sel_hi:[0,0,0]
	v_mfma_scale_f32_16x16x128_f8f6f4 v[108:111], v[186:193], v[210:217], v[108:111], v175, v176 op_sel_hi:[0,0,0]
	v_mfma_scale_f32_16x16x128_f8f6f4 v[104:107], v[178:185], v[218:225], v[104:107], v175, v176 op_sel_hi:[0,0,0]
	v_mfma_scale_f32_16x16x128_f8f6f4 v[100:103], v[186:193], v[218:225], v[100:103], v175, v176 op_sel_hi:[0,0,0]
	v_mfma_scale_f32_16x16x128_f8f6f4 v[96:99], v[178:185], v[226:233], v[96:99], v175, v176 op_sel_hi:[0,0,0]
	v_mfma_scale_f32_16x16x128_f8f6f4 v[92:95], v[186:193], v[226:233], v[92:95], v175, v176 op_sel_hi:[0,0,0]
	v_mfma_scale_f32_16x16x128_f8f6f4 v[88:91], v[0:7], v[202:209], v[88:91], v175, v176 op_sel_hi:[0,0,0]
	v_mfma_scale_f32_16x16x128_f8f6f4 v[84:87], v[194:201], v[202:209], v[84:87], v175, v176 op_sel_hi:[0,0,0]
	v_mfma_scale_f32_16x16x128_f8f6f4 v[80:83], v[0:7], v[210:217], v[80:83], v175, v176 op_sel_hi:[0,0,0]
	v_mfma_scale_f32_16x16x128_f8f6f4 v[76:79], v[194:201], v[210:217], v[76:79], v175, v176 op_sel_hi:[0,0,0]
	v_mfma_scale_f32_16x16x128_f8f6f4 v[72:75], v[0:7], v[218:225], v[72:75], v175, v176 op_sel_hi:[0,0,0]
	v_mfma_scale_f32_16x16x128_f8f6f4 v[68:71], v[194:201], v[218:225], v[68:71], v175, v176 op_sel_hi:[0,0,0]
	v_mfma_scale_f32_16x16x128_f8f6f4 v[64:67], v[0:7], v[226:233], v[64:67], v175, v176 op_sel_hi:[0,0,0]
	v_mfma_scale_f32_16x16x128_f8f6f4 v[60:63], v[194:201], v[226:233], v[60:63], v175, v176 op_sel_hi:[0,0,0]
	s_setprio 0
	s_barrier
	s_add_i32 s2, s2, s65
	v_lshl_add_u64 v[140:141], v[140:141], 0, s[26:27]
	s_mov_b32 m0, s2
	ds_read_b128 v[202:205], v174 offset:49152
	ds_read_b128 v[206:209], v174 offset:50176
	ds_read_b128 v[210:213], v174 offset:51200
	ds_read_b128 v[214:217], v174 offset:52224
	ds_read_b128 v[218:221], v174 offset:53248
	ds_read_b128 v[222:225], v174 offset:54272
	ds_read_b128 v[226:229], v174 offset:55296
	ds_read_b128 v[230:233], v174 offset:56320
	global_load_lds_dwordx4 v[140:141], off
	v_lshl_add_u64 v[140:141], v[142:143], 0, s[26:27]
	s_add_i32 m0, s2, 0x2000
	s_add_i32 s2, s3, s65
	global_load_lds_dwordx4 v[140:141], off
	v_lshl_add_u64 v[140:141], v[144:145], 0, s[26:27]
	s_mov_b32 m0, s2
	s_nop 0
	global_load_lds_dwordx4 v[140:141], off
	v_lshl_add_u64 v[140:141], v[146:147], 0, s[26:27]
	s_add_i32 m0, s2, 0x2000
	s_nop 0
	global_load_lds_dwordx4 v[140:141], off
	v_lshl_add_u64 v[140:141], v[148:149], 0, s[26:27]
	s_mov_b32 m0, s75
	s_nop 0
	global_load_lds_dwordx4 v[140:141], off
	v_lshl_add_u64 v[140:141], v[150:151], 0, s[26:27]
	s_mov_b32 m0, s76
	s_nop 0
	global_load_lds_dwordx4 v[140:141], off
	s_waitcnt vmcnt(8)
	s_waitcnt lgkmcnt(0)
	s_barrier
	s_setprio 1
	s_waitcnt lgkmcnt(0)
	v_mfma_scale_f32_16x16x128_f8f6f4 v[56:59], v[178:185], v[202:209], v[56:59], v175, v176 op_sel_hi:[0,0,0]
	v_mfma_scale_f32_16x16x128_f8f6f4 v[52:55], v[186:193], v[202:209], v[52:55], v175, v176 op_sel_hi:[0,0,0]
	v_mfma_scale_f32_16x16x128_f8f6f4 v[48:51], v[178:185], v[210:217], v[48:51], v175, v176 op_sel_hi:[0,0,0]
	v_mfma_scale_f32_16x16x128_f8f6f4 v[44:47], v[186:193], v[210:217], v[44:47], v175, v176 op_sel_hi:[0,0,0]
	v_mfma_scale_f32_16x16x128_f8f6f4 v[40:43], v[178:185], v[218:225], v[40:43], v175, v176 op_sel_hi:[0,0,0]
	v_mfma_scale_f32_16x16x128_f8f6f4 v[36:39], v[186:193], v[218:225], v[36:39], v175, v176 op_sel_hi:[0,0,0]
	v_mfma_scale_f32_16x16x128_f8f6f4 v[32:35], v[178:185], v[226:233], v[32:35], v175, v176 op_sel_hi:[0,0,0]
	v_mfma_scale_f32_16x16x128_f8f6f4 v[28:31], v[186:193], v[226:233], v[28:31], v175, v176 op_sel_hi:[0,0,0]
	v_mfma_scale_f32_16x16x128_f8f6f4 v[24:27], v[0:7], v[202:209], v[24:27], v175, v176 op_sel_hi:[0,0,0]
	v_mfma_scale_f32_16x16x128_f8f6f4 v[20:23], v[194:201], v[202:209], v[20:23], v175, v176 op_sel_hi:[0,0,0]
	v_mfma_scale_f32_16x16x128_f8f6f4 v[16:19], v[0:7], v[210:217], v[16:19], v175, v176 op_sel_hi:[0,0,0]
	v_mfma_scale_f32_16x16x128_f8f6f4 v[12:15], v[194:201], v[210:217], v[12:15], v175, v176 op_sel_hi:[0,0,0]
	v_mfma_scale_f32_16x16x128_f8f6f4 v[124:127], v[0:7], v[218:225], v[124:127], v175, v176 op_sel_hi:[0,0,0]
	v_mfma_scale_f32_16x16x128_f8f6f4 v[128:131], v[194:201], v[218:225], v[128:131], v175, v176 op_sel_hi:[0,0,0]
	v_mfma_scale_f32_16x16x128_f8f6f4 v[132:135], v[0:7], v[226:233], v[132:135], v175, v176 op_sel_hi:[0,0,0]
	v_mfma_scale_f32_16x16x128_f8f6f4 v[136:139], v[194:201], v[226:233], v[136:139], v175, v176 op_sel_hi:[0,0,0]
	s_setprio 0
	s_barrier
	s_add_u32 s52, s52, 0x100
	s_addc_u32 s53, s53, 0
	s_add_u32 s30, s30, 0x100
	s_addc_u32 s31, s31, 0
	s_cmp_ge_i32 s47, s73
	s_cbranch_scc1 .LBB0_1319
